# no tail-fill, own-layer conversion, 3-of-7 ticket pattern (conversions end at attention item 2048)
# baseline (speedup 1.0000x reference)
.LBB0_789:
	s_or_b64 exec, exec, s[2:3]
	v_readlane_b32 s2, v253, 55
	s_waitcnt lgkmcnt(0)
	s_barrier
	v_mov_b32_e32 v0, s2
	v_readlane_b32 s2, v253, 54
	ds_read_b32 v0, v0
	s_nop 0
	v_mov_b32_e32 v1, s2
	ds_read_b32 v1, v1
	s_waitcnt lgkmcnt(0)
	s_barrier
	v_add_u32_e32 v201, 0x580, v0
	s_nop 0
	v_readfirstlane_b32 s100, v201
	v_readlane_b32 s101, v254, 38
	s_nop 3
	s_movk_i32 vcc_lo, 0x600
	s_movk_i32 vcc_hi, 0xe00
	s_cmp_eq_u32 s101, 0
	s_cselect_b32 vcc_lo, 0x600, vcc_lo
	s_cselect_b32 vcc_hi, 0xe00, vcc_hi
	s_add_i32 vcc_lo, s100, vcc_lo
	s_max_u32 vcc_lo, vcc_lo, vcc_hi
	v_mov_b32_e32 v201, vcc_lo
	v_readfirstlane_b32 s30, v0
	v_cmp_ge_i32_e32 vcc, v1, v201
	v_readfirstlane_b32 s24, v1
	s_cbranch_vccnz .LBB0_931
	s_add_u32 s31, s4, 0x37b00000
	s_addc_u32 s34, s5, 0
	s_add_i32 s35, s30, 0x480
	s_add_u32 s44, s4, 0x61800000
	s_addc_u32 s45, s5, 0
	s_add_u32 s46, s4, 0x42c00000
	s_addc_u32 s47, s5, 0
	s_add_u32 s10, s4, 0x66d00000
	s_addc_u32 s11, s5, 0
	s_add_u32 s48, s4, 0x61640000
	s_movk_i32 s2, 0x100
	s_addc_u32 s49, s5, 0
	v_cmp_gt_i32_e64 s[38:39], s2, v199
	s_add_i32 s2, 0, 0x14800
	v_add_u32_e32 v214, s2, v200
	s_add_i32 s2, 0, 0x16800
	s_cmp_lg_u32 0, -1
	v_lshlrev_b32_e32 v3, 1, v199
	v_lshlrev_b32_e32 v211, 4, v199
	s_cselect_b32 s3, 0, 0
	v_lshlrev_b32_e32 v0, 3, v199
	v_lshlrev_b32_e32 v1, 10, v101
	v_lshlrev_b32_e32 v2, 4, v198
	v_and_b32_e32 v3, 32, v3
	v_and_b32_e32 v5, 0xc0, v211
	s_addk_i32 s3, 0x6000
	v_and_b32_e32 v210, 24, v0
	v_lshl_or_b32 v5, v101, 8, v5
	v_add3_u32 v213, 0, v1, v2
	v_add_u32_e32 v1, s3, v3
	v_add3_u32 v217, v1, v210, v5
	v_lshrrev_b32_e32 v1, 3, v100
	v_lshl_add_u32 v215, v198, 2, s2
	v_and_b32_e32 v218, 56, v0
	v_lshl_add_u32 v220, v1, 2, s2
	s_add_i32 s2, 0, 0x14a00
	v_add_u32_e32 v4, 0, v3
	v_lshlrev_b32_e32 v96, 1, v218
	v_add_u32_e32 v221, s2, v200
	s_add_i32 s2, 0, 0x14900
	v_ashrrev_i32_e32 v203, 31, v202
	v_lshlrev_b32_e32 v208, 9, v100
	v_lshrrev_b32_e32 v209, 2, v100
	v_add3_u32 v212, v4, v210, v5
	v_cmp_gt_u32_e64 s[40:41], 32, v100
	v_cmp_lt_u32_e64 s[42:43], 31, v100
	v_or_b32_e32 v216, 0xc0, v206
	v_lshl_add_u64 v[204:205], s[4:5], 0, v[96:97]
	v_lshlrev_b32_e32 v219, 7, v1
	v_add_u32_e32 v222, s2, v200
	v_lshlrev_b32_e32 v96, 1, v98
	s_branch .LBB0_792

.Lc3_pat:
	s_mul_i32 s101, s24, 0x2493
	s_lshr_b32 s101, s101, 16
	s_mul_i32 s2, s101, 7
	s_sub_i32 s2, s24, s2
	s_mul_i32 s101, s101, 3
	s_lshr_b32 vcc_lo, s2, 1
	s_add_i32 s101, s101, vcc_lo
	s_bitcmp1_b32 s2, 0
	s_cbranch_scc1 .Lc3_entry
	s_sub_i32 s24, s24, s101
	s_branch .Lc3_chk

.Lc3_l0:
	s_cmpk_lt_u32 s24, 0xe00
	s_cbranch_scc1 .Lc3_pat
